# attention: 4-stage K/V LDS ring, DMA fills three tiles ahead, next tile's K-fragment ds_reads issued right behind the QK^T MFMAs (no LDS latency at the tile top)
# baseline (speedup 1.0000x reference)
; #define LAS __attribute__((address_space(3)))
; #define AT_LOAD(j) do { _Pragma("unroll") for (int i = 0; i < 2; ++i) { const int id = tid + 512 * i, row = id >> 4, c16 = id & 15; \
;         rk[i] = *(const u32x4*)(kbase + (size_t)(64 * (j) + row) * PW + c16 * 8); rv[i] = *(const u32x4*)(vbase + (size_t)(64 * (j) + row) * PW + c16 * 8); } } while (0)
; #define AT_STORE(buf) do { _Pragma("unroll") for (int i = 0; i < 2; ++i) { const int id = tid + 512 * i, row = id >> 4, c16 = id & 15, mk = c16 >> 3, c = c16 & 7; \
;         *(LAS u32x4*)(lds + (buf) * STAGE + mk * 8192 + c * 1024 + ((row ^ c) * 16)) = rk[i]; \
;         *(LAS u32x4*)(lds + (buf) * STAGE + 16384 + (c16 >> 2) * 4096 + row * 64 + (c16 & 3) * 16) = rv[i]; } } while (0)
; __device__ __forceinline__ void attn_unit(const Frame& F, const bf16* __restrict__ proj, bf16* mix, const float* relb, const float* subg, int h, int qb, float lam, float one_m_li) {
;     ...
;     const int lane = tid & 63, w = F.wave, r32 = lane & 31, hi = lane >> 5, m = w >> 2, wq = w & 3;
;     const int q0 = qb * 128, qrow = q0 + 32 * wq + r32, cw = (q0 + 32 * wq) >> 6, NT = 2 * qb + 2;
;     LAS float* lut = (LAS float*)(lds + LDS_LUT);
;     if (tid < 256) { const int rel = tid - 192; lut[tid] = (relb[t5_bucket(rel) * 4 + h] - relb[15 * 4 + h]) * LOG2E; }
;     bf16x8 qr[4];
; #pragma unroll
;     for (int d0 = 0; d0 < 4; ++d0) qr[d0] = *(const bf16x8*)(proj + (size_t)qrow * PW + C_Q + h * 128 + m * 64 + 16 * d0 + 8 * hi);
;     u32x4 rk[2], rv[2];
;     const bf16* kbase = proj + C_K + h * 128; const bf16* vbase = proj + C_V + h * 128;
;     ...
;     AT_LOAD(0);
;     __syncthreads();
;     AT_STORE(0);
;     AT_LOAD(1);
;     __syncthreads();
.LBB0_573:
	s_or_b64 exec, exec, s[12:13]
	s_movk_i32 s12, 0xc0
	v_cmp_lt_i32_e32 vcc, s12, v32
	s_nop 1
	v_cndmask_b32_e64 v1, 0, 16, vcc
	v_add_lshl_u32 v192, v0, v1, 2
	v_lshl_add_u64 v[0:1], v[192:193], 2, s[46:47]
	global_load_dword v0, v[0:1], off
	s_nop 0
	global_load_dword v1, v193, s[46:47] offset:240
	s_waitcnt vmcnt(0)
	v_sub_f32_e32 v0, v0, v1
	v_lshl_add_u32 v1, v32, 2, 0
	v_mul_f32_e32 v0, 0x3fb8aa3b, v0
	v_add_u32_e32 v1, 0x20000, v1
	ds_write_b32 v1, v0
.LBB0_574:
	s_or_b64 exec, exec, s[10:11]
	s_lshr_b32 s101, s40, 10
	s_xor_b64 s[84:85], s[8:9], -1
	s_and_b64 s[8:9], s[8:9], exec
	s_cselect_b32 s8, s59, s58
	s_lshl_b32 s9, s8, 7
	v_and_b32_e32 v102, 31, v32
	s_or_b32 s9, s9, s29
	v_or_b32_e32 v188, s9, v102
	v_mul_u32_u24_e32 v0, 0x1200, v188
	v_lshlrev_b32_e32 v192, 1, v0
	v_lshl_add_u64 v[0:1], s[42:43], 0, v[192:193]
	v_bfe_u32 v187, v32, 5, 1
	v_lshl_add_u64 v[0:1], s[48:49], 1, v[0:1]
	v_lshl_add_u64 v[0:1], s[4:5], 1, v[0:1]
	v_lshlrev_b32_e32 v192, 4, v187
	v_lshl_add_u64 v[0:1], v[0:1], 0, v[192:193]
	s_mov_b64 s[10:11], 0x39101800
	v_lshl_add_u64 v[2:3], v[0:1], 0, s[10:11]
	s_mov_b32 s10, 0x39101000
	v_add_co_u32_e32 v0, vcc, s10, v0
	v_lshlrev_b32_e32 v33, 4, v32
	s_nop 0
	v_addc_co_u32_e32 v1, vcc, 0, v1, vcc
	v_and_b32_e32 v80, 0xf0, v33
	v_mov_b32_e32 v81, v193
	global_load_dwordx4 v[112:115], v[0:1], off offset:2048
	global_load_dwordx4 v[116:119], v[2:3], off offset:32
	global_load_dwordx4 v[120:123], v[2:3], off offset:64
	global_load_dwordx4 v[124:127], v[2:3], off offset:96
	v_lshl_add_u64 v[2:3], s[80:81], 0, v[80:81]
	v_lshl_add_u64 v[0:1], s[82:83], 0, v[80:81]
	v_ashrrev_i32_e32 v81, 4, v32
	v_mad_i64_i32 v[4:5], s[10:11], v81, s21, v[2:3]
	v_mad_i64_i32 v[8:9], s[10:11], v81, s21, v[0:1]
	v_add_u32_e32 v12, 0x200, v32
	v_ashrrev_i32_e32 v103, 4, v12
	v_mad_i64_i32 v[12:13], s[10:11], v103, s21, v[2:3]
	v_mad_i64_i32 v[16:17], s[10:11], v103, s21, v[0:1]
	v_and_b32_e32 v20, 7, v32
	v_lshlrev_b32_e32 v21, 10, v32
	v_mov_b32_e32 v189, 0
	v_lshlrev_b32_e32 v190, 8, v81
	v_bitop3_b32 v22, v81, v32, 15 bitop3:0x28
	v_add3_u32 v20, 0, v189, v190
	v_and_b32_e32 v191, 0x3000, v21
	v_and_b32_e32 v204, 48, v33
	v_lshlrev_b32_e32 v205, 4, v22
	v_add3_u32 v21, 0, v191, v204
	v_add_u32_e32 v22, v20, v205
	v_lshlrev_b32_e32 v206, 6, v81
	s_waitcnt lgkmcnt(0)
	s_barrier
	v_lshrrev_b32_e32 v4, 6, v32
	v_bfe_u32 v5, v32, 4, 2
	v_lshl_add_u32 v6, v4, 3, v5
	v_and_b32_e32 v7, 15, v32
	v_and_b32_e32 v8, 15, v6
	v_xor_b32_e32 v8, v7, v8
	v_mul_u32_u24_e32 v9, 0x2400, v6
	v_lshl_add_u32 v128, v8, 4, v9
	v_add_u32_e32 v6, 4, v6
	v_and_b32_e32 v8, 15, v6
	v_xor_b32_e32 v8, v7, v8
	v_mul_u32_u24_e32 v9, 0x2400, v6
	v_lshl_add_u32 v129, v8, 4, v9
	v_and_b32_e32 v5, 1, v4
	v_bfe_u32 v6, v32, 2, 4
	v_lshl_add_u32 v6, v5, 5, v6
	v_mul_u32_u24_e32 v9, 0x2400, v6
	v_lshrrev_b32_e32 v5, 1, v4
	v_lshl_add_u32 v9, v5, 6, v9
	v_and_b32_e32 v5, 3, v32
	v_lshl_add_u32 v9, v5, 4, v9
	v_add_u32_e32 v130, 0x400, v9
	v_add_u32_e32 v131, 0x24400, v9
	s_mov_b64 s[50:51], s[80:81]
	s_mov_b32 m0, s100
	s_nop 0
	global_load_lds_dwordx4 v128, s[50:51]
	s_add_i32 m0, s100, 0x400
	s_nop 0
	global_load_lds_dwordx4 v129, s[50:51]
	s_add_i32 m0, s100, 0x4000
	s_nop 0
	global_load_lds_dwordx4 v130, s[50:51]
	s_add_i32 m0, s100, 0x4400
	s_nop 0
	global_load_lds_dwordx4 v131, s[50:51]
	s_add_u32 s50, s50, 0x90000
	s_addc_u32 s51, s51, 0
	s_add_i32 m0, s100, 0x8000
	s_nop 0
	global_load_lds_dwordx4 v128, s[50:51]
	s_add_i32 m0, s100, 0x8400
	s_nop 0
	global_load_lds_dwordx4 v129, s[50:51]
	s_add_i32 m0, s100, 0xc000
	s_nop 0
	global_load_lds_dwordx4 v130, s[50:51]
	s_add_i32 m0, s100, 0xc400
	s_nop 0
	global_load_lds_dwordx4 v131, s[50:51]
	s_add_u32 s50, s50, 0x90000
	s_addc_u32 s51, s51, 0
	v_lshlrev_b32_e32 v208, 6, v103
	v_lshlrev_b32_e32 v209, 8, v102
	v_add_u32_e32 v6, v21, v206
	v_bitop3_b32 v4, v103, v32, 15 bitop3:0x28
	v_add_u32_e32 v9, 64, v81
	v_lshlrev_b32_e32 v207, 4, v4
	v_or_b32_e32 v207, 0x2000, v207
	v_mad_i64_i32 v[4:5], s[10:11], v9, s21, v[2:3]
	v_mad_i64_i32 v[4:5], s[10:11], v9, s21, v[0:1]
	v_add_u32_e32 v9, 64, v103
	v_mad_i64_i32 v[4:5], s[10:11], v9, s21, v[2:3]
	v_mad_i64_i32 v[4:5], s[10:11], v9, s21, v[0:1]
	v_bitop3_b32 v4, v187, v32, 15 bitop3:0x78
	v_xor_b32_e32 v4, s101, v4
	v_lshlrev_b32_e32 v210, 4, v4
	v_add_u32_e32 v7, v20, v207
	v_add_u32_e32 v8, v21, v208
	v_add3_u32 v4, 0, v209, v210
	s_waitcnt vmcnt(0)
	s_waitcnt lgkmcnt(0)
	s_barrier
	ds_read_b128 v[144:147], v4
	ds_read_b128 v[148:151], v4 offset:8192
	v_or_b32_e32 v4, 2, v187
	v_mov_b32_e32 v211, v209
	v_bitop3_b32 v4, v187, v32, 15 bitop3:0x78
	v_xor_b32_e32 v4, s101, v4
	v_xor_b32_e32 v4, 2, v4
	v_lshlrev_b32_e32 v212, 4, v4
	v_add3_u32 v4, 0, v211, v212
	ds_read_b128 v[152:155], v4
	ds_read_b128 v[156:159], v4 offset:8192
	s_cmp_eq_u32 s8, 0
	s_cbranch_scc1 .LBB0_576
	s_add_i32 m0, s100, 0x10000
	s_nop 0
	global_load_lds_dwordx4 v128, s[50:51]
	s_add_i32 m0, s100, 0x10400
	s_nop 0
	global_load_lds_dwordx4 v129, s[50:51]
	s_add_i32 m0, s100, 0x14000
	s_nop 0
	global_load_lds_dwordx4 v130, s[50:51]
	s_add_i32 m0, s100, 0x14400
	s_nop 0
	global_load_lds_dwordx4 v131, s[50:51]
	s_add_u32 s50, s50, 0x90000
	s_addc_u32 s51, s51, 0
	s_add_i32 m0, s100, 0x18000
	s_nop 0
	global_load_lds_dwordx4 v128, s[50:51]
	s_add_i32 m0, s100, 0x18400
	s_nop 0
	global_load_lds_dwordx4 v129, s[50:51]
	s_add_i32 m0, s100, 0x1c000
	s_nop 0
	global_load_lds_dwordx4 v130, s[50:51]
	s_add_i32 m0, s100, 0x1c400
	s_nop 0
	global_load_lds_dwordx4 v131, s[50:51]
	s_add_u32 s50, s50, 0x90000
	s_addc_u32 s51, s51, 0
; #define LAS __attribute__((address_space(3)))
; __device__ __forceinline__ int crow(int r, int hi) { return (r & 3) + 8 * (r >> 2) + 4 * hi; }
; #define AT_LOAD(j) do { _Pragma("unroll") for (int i = 0; i < 2; ++i) { const int id = tid + 512 * i, row = id >> 4, c16 = id & 15; \
;         rk[i] = *(const u32x4*)(kbase + (size_t)(64 * (j) + row) * PW + c16 * 8); rv[i] = *(const u32x4*)(vbase + (size_t)(64 * (j) + row) * PW + c16 * 8); } } while (0)
; #define AT_STORE(buf) do { _Pragma("unroll") for (int i = 0; i < 2; ++i) { const int id = tid + 512 * i, row = id >> 4, c16 = id & 15, mk = c16 >> 3, c = c16 & 7; \
;         *(LAS u32x4*)(lds + (buf) * STAGE + mk * 8192 + c * 1024 + ((row ^ c) * 16)) = rk[i]; \
;         *(LAS u32x4*)(lds + (buf) * STAGE + 16384 + (c16 >> 2) * 4096 + row * 64 + (c16 & 3) * 16) = rv[i]; } } while (0)
; __device__ __forceinline__ void attn_unit(const Frame& F, const bf16* __restrict__ proj, bf16* mix, const float* relb, const float* subg, int h, int qb, float lam, float one_m_li) {
;     ...
;         if (j <= cw) {
; #pragma unroll
;             for (int d0 = 0; d0 < 2; ++d0) { const int c = 2 * d0 + hi; kf[d0][0] = *(const LAS bf16x8*)(Kb + c * 1024 + ((r32 ^ c) * 16)); kf[d0][1] = *(const LAS bf16x8*)(Kb + c * 1024 + ((r32 ^ c) * 16) + 512); } }
;         __builtin_amdgcn_sched_barrier(0);
;         if (j + 1 < NT) AT_STORE(cur ^ 1);
;         if (j + 2 < NT) AT_LOAD(j + 2);
;         if (j <= cw) {
;             f32x16 p0, p1;
; #pragma unroll
;             for (int d0 = 0; d0 < 4; ++d0) { const int c = 2 * d0 + hi;
;                 const bf16x8 a0 = (d0 < 2) ? kf[d0 & 1][0] : *(const LAS bf16x8*)(Kb + c * 1024 + ((r32 ^ c) * 16));
;                 const bf16x8 a1 = (d0 < 2) ? kf[d0 & 1][1] : *(const LAS bf16x8*)(Kb + c * 1024 + ((r32 ^ c) * 16) + 512);
;                 if (d0 == 0) { p0 = __builtin_amdgcn_mfma_f32_32x32x16_bf16(a0, qr[0], negm, 0, 0, 0); p1 = __builtin_amdgcn_mfma_f32_32x32x16_bf16(a1, qr[0], negm, 0, 0, 0); }
;                 else { p0 = __builtin_amdgcn_mfma_f32_32x32x16_bf16(a0, qr[d0], p0, 0, 0, 0); p1 = __builtin_amdgcn_mfma_f32_32x32x16_bf16(a1, qr[d0], p1, 0, 0, 0); } }
;             if (j >= cw - 2) {
;                 const int base = 64 * j - qrow + 192;
; #pragma unroll
;                 for (int r = 0; r < 16; ++r) { const int kv = crow(r, hi); p0[r] += lut[base + kv]; p1[r] += lut[base + kv + 32]; }
.LBB0_576:
	s_waitcnt lgkmcnt(3)
	v_mfma_f32_32x32x16_bf16 v[0:15], v[144:147], v[112:115], 0
	v_or_b32_e32 v34, 4, v187
	v_mov_b32_e32 v214, v209
	v_bitop3_b32 v34, v187, v32, 15 bitop3:0x78
	v_xor_b32_e32 v34, s101, v34
	v_xor_b32_e32 v34, 4, v34
	v_lshlrev_b32_e32 v215, 4, v34
	v_add3_u32 v38, 0, v214, v215
	ds_read_b128 v[34:37], v38
	s_cmpk_gt_u32 s9, 0xbf
	s_waitcnt lgkmcnt(2)
	v_mfma_f32_32x32x16_bf16 v[0:15], v[152:155], v[116:119], v[0:15]
	v_mfma_f32_32x32x16_bf16 v[16:31], v[148:151], v[112:115], 0
	s_waitcnt lgkmcnt(0)
	v_mfma_f32_32x32x16_bf16 v[0:15], v[34:37], v[120:123], v[0:15]
	ds_read_b128 v[34:37], v38 offset:8192
	v_mfma_f32_32x32x16_bf16 v[16:31], v[156:159], v[116:119], v[16:31]
	s_waitcnt lgkmcnt(0)
	v_mfma_f32_32x32x16_bf16 v[16:31], v[34:37], v[120:123], v[16:31]
	v_or_b32_e32 v34, 6, v187
	v_mov_b32_e32 v216, v209
	v_bitop3_b32 v34, v187, v32, 15 bitop3:0x78
	v_xor_b32_e32 v34, s101, v34
	v_xor_b32_e32 v34, 6, v34
	v_lshlrev_b32_e32 v217, 4, v34
	v_add3_u32 v38, 0, v216, v217
	ds_read_b128 v[34:37], v38
	s_waitcnt lgkmcnt(0)
	v_mfma_f32_32x32x16_bf16 v[0:15], v[34:37], v[124:127], v[0:15]
	ds_read_b128 v[34:37], v38 offset:8192
	s_waitcnt lgkmcnt(0)
	v_mfma_f32_32x32x16_bf16 v[16:31], v[34:37], v[124:127], v[16:31]
	s_cbranch_scc1 .LBB0_578
	v_lshlrev_b32_e32 v34, 2, v188
	v_sub_u32_e32 v34, 0, v34
	v_add3_u32 v58, v34, v192, s75
	v_add_u32_e32 v58, 0x10000, v58
	ds_read2_b32 v[34:35], v58 offset0:192 offset1:193
	ds_read2_b32 v[36:37], v58 offset0:194 offset1:195
	ds_read2_b32 v[38:39], v58 offset0:200 offset1:201
	ds_read2_b32 v[40:41], v58 offset0:202 offset1:203
	ds_read2_b32 v[42:43], v58 offset0:208 offset1:209
	ds_read2_b32 v[44:45], v58 offset0:210 offset1:211
	ds_read2_b32 v[46:47], v58 offset0:216 offset1:217
	ds_read2_b32 v[48:49], v58 offset0:218 offset1:219
	ds_read2_b32 v[50:51], v58 offset0:224 offset1:225
	ds_read2_b32 v[52:53], v58 offset0:226 offset1:227
	ds_read2_b32 v[54:55], v58 offset0:232 offset1:233
	ds_read2_b32 v[56:57], v58 offset0:234 offset1:235
	s_waitcnt lgkmcnt(4)
	v_pk_add_f32 v[14:15], v[14:15], v[48:49]
	v_pk_add_f32 v[12:13], v[12:13], v[46:47]
	v_pk_add_f32 v[10:11], v[10:11], v[44:45]
	v_pk_add_f32 v[8:9], v[8:9], v[42:43]
	ds_read2_b32 v[42:43], v58 offset0:240 offset1:241
	ds_read2_b32 v[44:45], v58 offset0:242 offset1:243
	ds_read2_b32 v[46:47], v58 offset0:248 offset1:249
	ds_read2_b32 v[48:49], v58 offset0:250 offset1:251
	v_pk_add_f32 v[6:7], v[6:7], v[40:41]
	v_pk_add_f32 v[4:5], v[4:5], v[38:39]
	v_pk_add_f32 v[2:3], v[2:3], v[36:37]
	v_pk_add_f32 v[0:1], v[0:1], v[34:35]
	s_waitcnt lgkmcnt(0)
	v_pk_add_f32 v[30:31], v[30:31], v[48:49]
	v_pk_add_f32 v[28:29], v[28:29], v[46:47]
	v_pk_add_f32 v[26:27], v[26:27], v[44:45]
	v_pk_add_f32 v[24:25], v[24:25], v[42:43]
	v_pk_add_f32 v[22:23], v[22:23], v[56:57]
	v_pk_add_f32 v[20:21], v[20:21], v[54:55]
	v_pk_add_f32 v[18:19], v[18:19], v[52:53]
	v_pk_add_f32 v[16:17], v[16:17], v[50:51]

; #define LAS __attribute__((address_space(3)))
; __device__ __forceinline__ void attn_unit(const Frame& F, const bf16* __restrict__ proj, bf16* mix, const float* relb, const float* subg, int h, int qb, float lam, float one_m_li) {
;     ...
;         if (j <= cw) {
; #pragma unroll
;             for (int d0 = 0; d0 < 2; ++d0) { const int c = 2 * d0 + hi; kf[d0][0] = *(const LAS bf16x8*)(Kb + c * 1024 + ((r32 ^ c) * 16)); kf[d0][1] = *(const LAS bf16x8*)(Kb + c * 1024 + ((r32 ^ c) * 16) + 512); } }
.Ldma_pwd:
	s_mov_b32 s101, 0x8000
	v_add3_u32 v170, s101, v209, v210
	v_add3_u32 v171, s101, v211, v212
	v_add3_u32 v172, s101, v214, v215
	v_add3_u32 v173, s101, v216, v217
	ds_read_b128 v[144:147], v170
	ds_read_b128 v[148:151], v170 offset:8192
	ds_read_b128 v[152:155], v171
	ds_read_b128 v[156:159], v171 offset:8192
	ds_read_b128 v[132:135], v172
	ds_read_b128 v[136:139], v172 offset:8192
	ds_read_b128 v[140:143], v173
	ds_read_b128 v[164:167], v173 offset:8192
	s_barrier
	s_branch .LBB0_581

; #define LAS __attribute__((address_space(3)))
; #define AT_LOAD(j) do { _Pragma("unroll") for (int i = 0; i < 2; ++i) { const int id = tid + 512 * i, row = id >> 4, c16 = id & 15; \
;         rk[i] = *(const u32x4*)(kbase + (size_t)(64 * (j) + row) * PW + c16 * 8); rv[i] = *(const u32x4*)(vbase + (size_t)(64 * (j) + row) * PW + c16 * 8); } } while (0)
; #define AT_STORE(buf) do { _Pragma("unroll") for (int i = 0; i < 2; ++i) { const int id = tid + 512 * i, row = id >> 4, c16 = id & 15, mk = c16 >> 3, c = c16 & 7; \
;         *(LAS u32x4*)(lds + (buf) * STAGE + mk * 8192 + c * 1024 + ((row ^ c) * 16)) = rk[i]; \
;         *(LAS u32x4*)(lds + (buf) * STAGE + 16384 + (c16 >> 2) * 4096 + row * 64 + (c16 & 3) * 16) = rv[i]; } } while (0)
; __device__ __forceinline__ void attn_unit(const Frame& F, const bf16* __restrict__ proj, bf16* mix, const float* relb, const float* subg, int h, int qb, float lam, float one_m_li) {
;     ...
;     for (int j = 0; j < NT; ++j) {
;         const int cur = j & 1;
;         bf16x8 kf[2][2];
;         const LAS unsigned char* Kb = lds + cur * STAGE + m * 8192;
;         if (j <= cw) {
; #pragma unroll
;             for (int d0 = 0; d0 < 2; ++d0) { const int c = 2 * d0 + hi; kf[d0][0] = *(const LAS bf16x8*)(Kb + c * 1024 + ((r32 ^ c) * 16)); kf[d0][1] = *(const LAS bf16x8*)(Kb + c * 1024 + ((r32 ^ c) * 16) + 512); } }
;         __builtin_amdgcn_sched_barrier(0);
;         if (j + 1 < NT) AT_STORE(cur ^ 1);
;         if (j + 2 < NT) AT_LOAD(j + 2);
.LBB0_580:
	s_addk_i32 s60, 0x100
	s_add_i32 s73, s73, 0x8000
	s_cmp_eq_u32 s73, 0x20000
	s_cselect_b32 s73, 0, s73
	s_add_i32 s13, s13, 1
	s_add_i32 s101, s12, -1
	s_cmp_ge_i32 s86, s101
	s_cbranch_scc1 .Ldma_w0
	s_waitcnt vmcnt(4) lgkmcnt(0)
	s_branch .Ldma_wd

; #define LAS __attribute__((address_space(3)))
; __device__ __forceinline__ int crow(int r, int hi) { return (r & 3) + 8 * (r >> 2) + 4 * hi; }
; #define AT_LOAD(j) do { _Pragma("unroll") for (int i = 0; i < 2; ++i) { const int id = tid + 512 * i, row = id >> 4, c16 = id & 15; \
;         rk[i] = *(const u32x4*)(kbase + (size_t)(64 * (j) + row) * PW + c16 * 8); rv[i] = *(const u32x4*)(vbase + (size_t)(64 * (j) + row) * PW + c16 * 8); } } while (0)
; #define AT_STORE(buf) do { _Pragma("unroll") for (int i = 0; i < 2; ++i) { const int id = tid + 512 * i, row = id >> 4, c16 = id & 15, mk = c16 >> 3, c = c16 & 7; \
;         *(LAS u32x4*)(lds + (buf) * STAGE + mk * 8192 + c * 1024 + ((row ^ c) * 16)) = rk[i]; \
;         *(LAS u32x4*)(lds + (buf) * STAGE + 16384 + (c16 >> 2) * 4096 + row * 64 + (c16 & 3) * 16) = rv[i]; } } while (0)
; __device__ __forceinline__ void attn_unit(const Frame& F, const bf16* __restrict__ proj, bf16* mix, const float* relb, const float* subg, int h, int qb, float lam, float one_m_li) {
;     ...
;         if (j <= cw) {
; #pragma unroll
;             for (int d0 = 0; d0 < 2; ++d0) { const int c = 2 * d0 + hi; kf[d0][0] = *(const LAS bf16x8*)(Kb + c * 1024 + ((r32 ^ c) * 16)); kf[d0][1] = *(const LAS bf16x8*)(Kb + c * 1024 + ((r32 ^ c) * 16) + 512); } }
;         __builtin_amdgcn_sched_barrier(0);
;         if (j + 1 < NT) AT_STORE(cur ^ 1);
;         if (j + 2 < NT) AT_LOAD(j + 2);
;         if (j <= cw) {
;             f32x16 p0, p1;
; #pragma unroll
;             for (int d0 = 0; d0 < 4; ++d0) { const int c = 2 * d0 + hi;
;                 const bf16x8 a0 = (d0 < 2) ? kf[d0 & 1][0] : *(const LAS bf16x8*)(Kb + c * 1024 + ((r32 ^ c) * 16));
;                 const bf16x8 a1 = (d0 < 2) ? kf[d0 & 1][1] : *(const LAS bf16x8*)(Kb + c * 1024 + ((r32 ^ c) * 16) + 512);
;                 if (d0 == 0) { p0 = __builtin_amdgcn_mfma_f32_32x32x16_bf16(a0, qr[0], negm, 0, 0, 0); p1 = __builtin_amdgcn_mfma_f32_32x32x16_bf16(a1, qr[0], negm, 0, 0, 0); }
;                 else { p0 = __builtin_amdgcn_mfma_f32_32x32x16_bf16(a0, qr[d0], p0, 0, 0, 0); p1 = __builtin_amdgcn_mfma_f32_32x32x16_bf16(a1, qr[d0], p1, 0, 0, 0); } }
;             if (j >= cw - 2) {
;                 const int base = 64 * j - qrow + 192;
; #pragma unroll
;                 for (int r = 0; r < 16; ++r) { const int kv = crow(r, hi); p0[r] += lut[base + kv]; p1[r] += lut[base + kv + 32]; }
.LBB0_581:
	s_mov_b32 s88, s73
	s_add_i32 s79, s88, 0
	s_add_i32 s86, s13, -1
	s_add_i32 s87, s79, s40
	s_add_i32 s101, s12, -1
	s_cmp_ge_i32 s86, s101
	s_cbranch_scc1 .Ldma_skip
	s_sub_i32 s101, s88, 0x8000
	s_cmp_eq_u32 s88, 0
	s_cselect_b32 s101, 0x18000, s101
	s_add_i32 s101, s101, s100
	s_mov_b32 m0, s101
	s_nop 0
	global_load_lds_dwordx4 v128, s[50:51]
	s_add_i32 m0, s101, 0x400
	s_nop 0
	global_load_lds_dwordx4 v129, s[50:51]
	s_add_i32 m0, s101, 0x4000
	s_nop 0
	global_load_lds_dwordx4 v130, s[50:51]
	s_add_i32 m0, s101, 0x4400
	s_nop 0
	global_load_lds_dwordx4 v131, s[50:51]
	s_add_u32 s50, s50, 0x90000
	s_addc_u32 s51, s51, 0
.Ldma_skip:
	s_cmp_gt_u32 s86, s10
	s_cbranch_scc1 .LBB0_580
	s_waitcnt lgkmcnt(7)
	v_mfma_f32_32x32x16_bf16 v[96:111], v[144:147], v[112:115], v[64:79]
	s_waitcnt lgkmcnt(6)
	v_mfma_f32_32x32x16_bf16 v[80:95], v[148:151], v[112:115], v[64:79]
	s_waitcnt lgkmcnt(5)
	v_mfma_f32_32x32x16_bf16 v[96:111], v[152:155], v[116:119], v[96:111]
	s_waitcnt lgkmcnt(4)
	v_mfma_f32_32x32x16_bf16 v[80:95], v[156:159], v[116:119], v[80:95]
	s_waitcnt lgkmcnt(3)
	v_mfma_f32_32x32x16_bf16 v[96:111], v[132:135], v[120:123], v[96:111]
	s_waitcnt lgkmcnt(2)
	v_mfma_f32_32x32x16_bf16 v[80:95], v[136:139], v[120:123], v[80:95]
	s_waitcnt lgkmcnt(1)
	v_mfma_f32_32x32x16_bf16 v[96:111], v[140:143], v[124:127], v[96:111]
	s_waitcnt lgkmcnt(0)
	v_mfma_f32_32x32x16_bf16 v[80:95], v[164:167], v[124:127], v[80:95]
	s_cmp_lt_i32 s86, s11
	s_cbranch_scc1 .LBB0_590
	v_add_u32_e32 v223, s60, v222
	v_add_u32_e32 v168, 0x20500, v223
	v_add_u32_e32 v170, 0x20580, v223
	ds_read2_b32 v[168:169], v168 offset1:1
	ds_read2_b32 v[170:171], v170 offset1:1
	v_add_u32_e32 v172, 0x20508, v223
	v_add_u32_e32 v174, 0x20588, v223
	v_add_u32_e32 v176, 0x20520, v223
	v_add_u32_e32 v178, 0x205a0, v223
	v_add_u32_e32 v180, 0x20528, v223
	v_add_u32_e32 v182, 0x205a8, v223
	v_add_u32_e32 v184, 0x20540, v223
	v_add_u32_e32 v196, 0x205c0, v223
	v_add_u32_e32 v198, 0x20548, v223
	v_add_u32_e32 v200, 0x205c8, v223
	v_add_u32_e32 v202, 0x20560, v223
	v_add_u32_e32 v224, 0x205e0, v223
	v_add_u32_e32 v226, 0x20568, v223
	v_add_u32_e32 v223, 0x205e8, v223
	ds_read2_b32 v[172:173], v172 offset1:1
	ds_read2_b32 v[174:175], v174 offset1:1
	ds_read2_b32 v[176:177], v176 offset1:1
	ds_read2_b32 v[178:179], v178 offset1:1
	ds_read2_b32 v[180:181], v180 offset1:1
	ds_read2_b32 v[182:183], v182 offset1:1
	ds_read2_b32 v[184:185], v184 offset1:1
	ds_read2_b32 v[196:197], v196 offset1:1
	ds_read2_b32 v[198:199], v198 offset1:1
	ds_read2_b32 v[200:201], v200 offset1:1
	ds_read2_b32 v[202:203], v202 offset1:1
	ds_read2_b32 v[224:225], v224 offset1:1
	ds_read2_b32 v[226:227], v226 offset1:1
	s_waitcnt lgkmcnt(14)
	v_pk_add_f32 v[96:97], v[96:97], v[168:169]
	ds_read2_b32 v[168:169], v223 offset1:1
	s_waitcnt lgkmcnt(3)
	v_pk_add_f32 v[108:109], v[108:109], v[202:203]
	v_pk_add_f32 v[106:107], v[106:107], v[198:199]
	s_waitcnt lgkmcnt(1)
	v_pk_add_f32 v[110:111], v[110:111], v[226:227]
	v_pk_add_f32 v[104:105], v[104:105], v[184:185]
	v_pk_add_f32 v[102:103], v[102:103], v[180:181]
	v_pk_add_f32 v[100:101], v[100:101], v[176:177]
	v_pk_add_f32 v[98:99], v[98:99], v[172:173]
	s_waitcnt lgkmcnt(0)
	v_pk_add_f32 v[94:95], v[94:95], v[168:169]
	v_pk_add_f32 v[92:93], v[92:93], v[224:225]
	v_pk_add_f32 v[90:91], v[90:91], v[200:201]
	v_pk_add_f32 v[88:89], v[88:89], v[196:197]
	v_pk_add_f32 v[86:87], v[86:87], v[182:183]
	v_pk_add_f32 v[84:85], v[84:85], v[178:179]
	v_pk_add_f32 v[82:83], v[82:83], v[174:175]
	v_pk_add_f32 v[80:81], v[80:81], v[170:171]
; __device__ __forceinline__ float swap_max(float v) { float r0, r1; swap32(v, r0, r1); return fmaxf(r0, r1); }
; __device__ __forceinline__ void attn_unit(const Frame& F, const bf16* __restrict__ proj, bf16* mix, const float* relb, const float* subg, int h, int qb, float lam, float one_m_li) {
;     ...
;             float mx = fmaxf(fmaxf(p0[0], p0[1]), p1[0]), mb = fmaxf(fmaxf(p0[2], p0[3]), p1[1]); mx = fmaxf(fmaxf(mx, p1[2]), p1[3]);
; #pragma unroll
;             for (int r = 4; r < 16; r += 4) { mx = fmaxf(fmaxf(mx, p0[r]), p0[r + 1]); mb = fmaxf(fmaxf(mb, p0[r + 2]), p0[r + 3]); mx = fmaxf(fmaxf(mx, p1[r]), p1[r + 1]); mb = fmaxf(fmaxf(mb, p1[r + 2]), p1[r + 3]); }
;             mx = swap_max(fmaxf(mx, mb));
;             if (j == 0 || __any(mx > 8.0f)) {
;                 const float dl = (j == 0) ? mx : fmaxf(mx, 0.f); mrun += dl;
;                 const float alpha = __builtin_amdgcn_exp2f(-dl); lsum *= alpha;
; #pragma unroll
;                 for (int r = 0; r < 16; ++r) { p0[r] -= dl; p1[r] -= dl; negm[r] = -mrun; }
; #pragma unroll
;                 for (int eb = 0; eb < 4; ++eb)
; #pragma unroll
;                     for (int r = 0; r < 16; ++r) o[eb][r] *= alpha;
;             }
.LBB0_590:
	s_add_i32 s101, s88, 0x8000
	s_cmp_eq_u32 s101, 0x20000
	s_cselect_b32 s101, 0, s101
	v_add3_u32 v170, s101, v209, v210
	v_add3_u32 v171, s101, v211, v212
	v_add3_u32 v172, s101, v214, v215
	v_add3_u32 v173, s101, v216, v217
	ds_read_b128 v[144:147], v170
	ds_read_b128 v[148:151], v170 offset:8192
	ds_read_b128 v[152:155], v171
	ds_read_b128 v[156:159], v171 offset:8192
	ds_read_b128 v[132:135], v172
	ds_read_b128 v[136:139], v172 offset:8192
	ds_read_b128 v[140:143], v173
	ds_read_b128 v[164:167], v173 offset:8192
	v_max_f32_e32 v168, v97, v97
	v_max_f32_e32 v169, v96, v96
	v_max_f32_e32 v168, v169, v168
	v_max3_f32 v169, v98, v99, v81
	v_max3_f32 v168, v168, v80, v82
	v_max3_f32 v168, v168, v83, v100
	v_max3_f32 v169, v169, v102, v103
	v_max3_f32 v168, v168, v101, v84
	v_max3_f32 v169, v169, v86, v87
	v_max3_f32 v168, v168, v85, v104
	v_max3_f32 v169, v169, v106, v107
	v_max3_f32 v168, v168, v105, v88
	v_max3_f32 v169, v169, v90, v91
	v_max3_f32 v168, v168, v89, v108
	v_max3_f32 v169, v169, v110, v111
	v_max3_f32 v168, v168, v109, v92
	v_max3_f32 v169, v169, v94, v95
	v_max3_f32 v168, v168, v93, v169
	v_mov_b32_e32 v169, v168
	s_nop 1
	v_permlane32_swap_b32 v168, v169
	s_mov_b32 s8, 0x41000000
	v_max_f32_e32 v169, v169, v169
	v_max_f32_e32 v168, v168, v168
	v_max_f32_e32 v168, v168, v169
	v_cmp_lt_f32_e32 vcc, s8, v168
	s_cbranch_vccz .LBB0_579
	v_max_f32_e32 v64, v168, v168
	v_max_f32_e32 v66, 0, v64
	v_exp_f32_e64 v68, -v66
	v_add_f32_e32 v162, v162, v66
	v_xor_b32_e32 v64, 0x80000000, v162
	v_pk_add_f32 v[96:97], v[96:97], v[66:67] op_sel_hi:[1,0] neg_lo:[0,1] neg_hi:[0,1]
	v_pk_add_f32 v[80:81], v[80:81], v[66:67] op_sel_hi:[1,0] neg_lo:[0,1] neg_hi:[0,1]
	v_pk_add_f32 v[98:99], v[98:99], v[66:67] op_sel_hi:[1,0] neg_lo:[0,1] neg_hi:[0,1]
	v_pk_add_f32 v[82:83], v[82:83], v[66:67] op_sel_hi:[1,0] neg_lo:[0,1] neg_hi:[0,1]
	v_pk_add_f32 v[100:101], v[100:101], v[66:67] op_sel_hi:[1,0] neg_lo:[0,1] neg_hi:[0,1]
	v_pk_add_f32 v[84:85], v[84:85], v[66:67] op_sel_hi:[1,0] neg_lo:[0,1] neg_hi:[0,1]
	v_pk_add_f32 v[102:103], v[102:103], v[66:67] op_sel_hi:[1,0] neg_lo:[0,1] neg_hi:[0,1]
	v_pk_add_f32 v[86:87], v[86:87], v[66:67] op_sel_hi:[1,0] neg_lo:[0,1] neg_hi:[0,1]
	v_pk_add_f32 v[104:105], v[104:105], v[66:67] op_sel_hi:[1,0] neg_lo:[0,1] neg_hi:[0,1]
	v_pk_add_f32 v[88:89], v[88:89], v[66:67] op_sel_hi:[1,0] neg_lo:[0,1] neg_hi:[0,1]
	v_pk_add_f32 v[106:107], v[106:107], v[66:67] op_sel_hi:[1,0] neg_lo:[0,1] neg_hi:[0,1]
	v_pk_add_f32 v[90:91], v[90:91], v[66:67] op_sel_hi:[1,0] neg_lo:[0,1] neg_hi:[0,1]
	v_pk_add_f32 v[108:109], v[108:109], v[66:67] op_sel_hi:[1,0] neg_lo:[0,1] neg_hi:[0,1]
	v_pk_add_f32 v[92:93], v[92:93], v[66:67] op_sel_hi:[1,0] neg_lo:[0,1] neg_hi:[0,1]
	v_pk_add_f32 v[110:111], v[110:111], v[66:67] op_sel_hi:[1,0] neg_lo:[0,1] neg_hi:[0,1]
	v_pk_add_f32 v[94:95], v[94:95], v[66:67] op_sel_hi:[1,0] neg_lo:[0,1] neg_hi:[0,1]
	v_pk_mul_f32 v[62:63], v[62:63], v[68:69] op_sel_hi:[1,0]
	v_pk_mul_f32 v[60:61], v[60:61], v[68:69] op_sel_hi:[1,0]
	v_pk_mul_f32 v[58:59], v[58:59], v[68:69] op_sel_hi:[1,0]
	v_pk_mul_f32 v[56:57], v[56:57], v[68:69] op_sel_hi:[1,0]
	v_pk_mul_f32 v[54:55], v[54:55], v[68:69] op_sel_hi:[1,0]
	v_pk_mul_f32 v[52:53], v[52:53], v[68:69] op_sel_hi:[1,0]
	v_pk_mul_f32 v[50:51], v[50:51], v[68:69] op_sel_hi:[1,0]
	v_pk_mul_f32 v[48:49], v[48:49], v[68:69] op_sel_hi:[1,0]
	v_pk_mul_f32 v[46:47], v[46:47], v[68:69] op_sel_hi:[1,0]
	v_pk_mul_f32 v[44:45], v[44:45], v[68:69] op_sel_hi:[1,0]
	v_pk_mul_f32 v[42:43], v[42:43], v[68:69] op_sel_hi:[1,0]
	v_pk_mul_f32 v[40:41], v[40:41], v[68:69] op_sel_hi:[1,0]
	v_pk_mul_f32 v[38:39], v[38:39], v[68:69] op_sel_hi:[1,0]
	v_pk_mul_f32 v[36:37], v[36:37], v[68:69] op_sel_hi:[1,0]
	v_pk_mul_f32 v[34:35], v[34:35], v[68:69] op_sel_hi:[1,0]
	v_pk_mul_f32 v[32:33], v[32:33], v[68:69] op_sel_hi:[1,0]
	v_pk_mul_f32 v[30:31], v[30:31], v[68:69] op_sel_hi:[1,0]
	v_pk_mul_f32 v[28:29], v[28:29], v[68:69] op_sel_hi:[1,0]
	v_pk_mul_f32 v[26:27], v[26:27], v[68:69] op_sel_hi:[1,0]
	v_pk_mul_f32 v[24:25], v[24:25], v[68:69] op_sel_hi:[1,0]
	v_pk_mul_f32 v[22:23], v[22:23], v[68:69] op_sel_hi:[1,0]
	v_pk_mul_f32 v[20:21], v[20:21], v[68:69] op_sel_hi:[1,0]
	v_pk_mul_f32 v[18:19], v[18:19], v[68:69] op_sel_hi:[1,0]
	v_pk_mul_f32 v[16:17], v[16:17], v[68:69] op_sel_hi:[1,0]
	v_pk_mul_f32 v[14:15], v[14:15], v[68:69] op_sel_hi:[1,0]
	v_pk_mul_f32 v[12:13], v[12:13], v[68:69] op_sel_hi:[1,0]
	v_pk_mul_f32 v[10:11], v[10:11], v[68:69] op_sel_hi:[1,0]
	v_pk_mul_f32 v[8:9], v[8:9], v[68:69] op_sel_hi:[1,0]
	v_pk_mul_f32 v[6:7], v[6:7], v[68:69] op_sel_hi:[1,0]
	v_pk_mul_f32 v[4:5], v[4:5], v[68:69] op_sel_hi:[1,0]
	v_pk_mul_f32 v[2:3], v[2:3], v[68:69] op_sel_hi:[1,0]
	v_pk_mul_f32 v[0:1], v[0:1], v[68:69] op_sel_hi:[1,0]
	v_mul_f32_e32 v163, v163, v68
	v_mov_b32_e32 v65, v64
	v_mov_b32_e32 v66, v64
	v_mov_b32_e32 v67, v64
	v_mov_b32_e32 v68, v64
	v_mov_b32_e32 v69, v64
	v_mov_b32_e32 v70, v64
	v_mov_b32_e32 v71, v64
	v_mov_b32_e32 v72, v64
	v_mov_b32_e32 v73, v64
	v_mov_b32_e32 v74, v64
	v_mov_b32_e32 v75, v64
	v_mov_b32_e32 v76, v64
	v_mov_b32_e32 v77, v64
	v_mov_b32_e32 v78, v64
	v_mov_b32_e32 v79, v64
	s_branch .LBB0_579
